# speedup vs baseline: 1.0050x; 1.0050x over previous
.Lagg_gmaxret_1:
	s_mov_b64 exec, s[66:67]
	v_fma_mix_f32 v32, v48, v42, 0 op_sel_hi:[1,0,0]
	v_fma_mix_f32 v33, v48, v42, 0 op_sel:[1,0,0] op_sel_hi:[1,0,0]
	v_fma_mix_f32 v34, v49, v42, 0 op_sel_hi:[1,0,0]
	v_fma_mix_f32 v35, v49, v42, 0 op_sel:[1,0,0] op_sel_hi:[1,0,0]
	v_fma_mix_f32 v36, v50, v42, 0 op_sel_hi:[1,0,0]
	v_fma_mix_f32 v37, v50, v42, 0 op_sel:[1,0,0] op_sel_hi:[1,0,0]
	v_fma_mix_f32 v38, v51, v42, 0 op_sel_hi:[1,0,0]
	v_fma_mix_f32 v39, v51, v42, 0 op_sel:[1,0,0] op_sel_hi:[1,0,0]
	v_fma_mix_f32 v56, v52, v42, 0 op_sel_hi:[1,0,0]
	v_fma_mix_f32 v57, v52, v42, 0 op_sel:[1,0,0] op_sel_hi:[1,0,0]
	v_fma_mix_f32 v58, v53, v42, 0 op_sel_hi:[1,0,0]
	v_fma_mix_f32 v59, v53, v42, 0 op_sel:[1,0,0] op_sel_hi:[1,0,0]
	v_fma_mix_f32 v60, v54, v42, 0 op_sel_hi:[1,0,0]
	v_fma_mix_f32 v61, v54, v42, 0 op_sel:[1,0,0] op_sel_hi:[1,0,0]
	v_fma_mix_f32 v62, v55, v42, 0 op_sel_hi:[1,0,0]
	v_fma_mix_f32 v63, v55, v42, 0 op_sel:[1,0,0] op_sel_hi:[1,0,0]
	v_fma_mix_f32 v32, v5, v15, v32 op_sel_hi:[1,0,0]
	v_fma_mix_f32 v33, v5, v15, v33 op_sel:[1,0,0] op_sel_hi:[1,0,0]
	v_fma_mix_f32 v34, v6, v15, v34 op_sel_hi:[1,0,0]
	v_fma_mix_f32 v35, v6, v15, v35 op_sel:[1,0,0] op_sel_hi:[1,0,0]
	v_fma_mix_f32 v36, v7, v15, v36 op_sel_hi:[1,0,0]
	v_fma_mix_f32 v37, v7, v15, v37 op_sel:[1,0,0] op_sel_hi:[1,0,0]
	v_fma_mix_f32 v38, v8, v15, v38 op_sel_hi:[1,0,0]
	v_fma_mix_f32 v39, v8, v15, v39 op_sel:[1,0,0] op_sel_hi:[1,0,0]
	v_fma_mix_f32 v56, v9, v15, v56 op_sel_hi:[1,0,0]
	v_fma_mix_f32 v57, v9, v15, v57 op_sel:[1,0,0] op_sel_hi:[1,0,0]
	v_fma_mix_f32 v58, v10, v15, v58 op_sel_hi:[1,0,0]
	v_fma_mix_f32 v59, v10, v15, v59 op_sel:[1,0,0] op_sel_hi:[1,0,0]
	v_fma_mix_f32 v60, v11, v15, v60 op_sel_hi:[1,0,0]
	v_fma_mix_f32 v61, v11, v15, v61 op_sel:[1,0,0] op_sel_hi:[1,0,0]
	v_fma_mix_f32 v62, v12, v15, v62 op_sel_hi:[1,0,0]
	v_fma_mix_f32 v63, v12, v15, v63 op_sel:[1,0,0] op_sel_hi:[1,0,0]
	s_waitcnt vmcnt(1)
	v_fma_mix_f32 v32, v24, v15, v32 op_sel_hi:[1,0,0]
	v_fma_mix_f32 v33, v24, v15, v33 op_sel:[1,0,0] op_sel_hi:[1,0,0]
	v_fma_mix_f32 v34, v25, v15, v34 op_sel_hi:[1,0,0]
	v_fma_mix_f32 v35, v25, v15, v35 op_sel:[1,0,0] op_sel_hi:[1,0,0]
	v_fma_mix_f32 v36, v26, v15, v36 op_sel_hi:[1,0,0]
	v_fma_mix_f32 v37, v26, v15, v37 op_sel:[1,0,0] op_sel_hi:[1,0,0]
	v_fma_mix_f32 v38, v27, v15, v38 op_sel_hi:[1,0,0]
	v_fma_mix_f32 v39, v27, v15, v39 op_sel:[1,0,0] op_sel_hi:[1,0,0]
	s_waitcnt vmcnt(0)
	v_fma_mix_f32 v56, v28, v15, v56 op_sel_hi:[1,0,0]
	v_fma_mix_f32 v57, v28, v15, v57 op_sel:[1,0,0] op_sel_hi:[1,0,0]
	v_fma_mix_f32 v58, v29, v15, v58 op_sel_hi:[1,0,0]
	v_fma_mix_f32 v59, v29, v15, v59 op_sel:[1,0,0] op_sel_hi:[1,0,0]
	v_fma_mix_f32 v60, v30, v15, v60 op_sel_hi:[1,0,0]
	v_fma_mix_f32 v61, v30, v15, v61 op_sel:[1,0,0] op_sel_hi:[1,0,0]
	v_fma_mix_f32 v62, v31, v15, v62 op_sel_hi:[1,0,0]
	v_fma_mix_f32 v63, v31, v15, v63 op_sel:[1,0,0] op_sel_hi:[1,0,0]
	v_max_f32_e32 v32, 0, v32
	v_max_f32_e32 v33, 0, v33
	v_max_f32_e32 v34, 0, v34
	v_max_f32_e32 v35, 0, v35
	v_max_f32_e32 v36, 0, v36
	v_max_f32_e32 v37, 0, v37
	v_max_f32_e32 v38, 0, v38
	v_max_f32_e32 v39, 0, v39
	v_max_f32_e32 v56, 0, v56
	v_max_f32_e32 v57, 0, v57
	v_max_f32_e32 v58, 0, v58
	v_max_f32_e32 v59, 0, v59
	v_max_f32_e32 v60, 0, v60
	v_max_f32_e32 v61, 0, v61
	v_max_f32_e32 v62, 0, v62
	v_max_f32_e32 v63, 0, v63
	v_lshlrev_b32_e32 v40, 2, v0
	v_add_u32_e32 v44, 0x6200, v40
	ds_write_b32 v40, v32 offset:24448
	ds_write_b32 v40, v33 offset:27584
	ds_write_b32 v40, v34 offset:30720
	ds_write_b32 v40, v35 offset:33856
	ds_write_b32 v40, v36 offset:36992
	ds_write_b32 v40, v37 offset:40128
	ds_write_b32 v40, v38 offset:43264
	ds_write_b32 v40, v39 offset:46400
	ds_write_b32 v44, v56 offset:24448
	ds_write_b32 v44, v57 offset:27584
	ds_write_b32 v44, v58 offset:30720
	ds_write_b32 v44, v59 offset:33856
	ds_write_b32 v44, v60 offset:36992
	ds_write_b32 v44, v61 offset:40128
	ds_write_b32 v44, v62 offset:43264
	ds_write_b32 v44, v63 offset:46400
	v_lshrrev_b32_e32 v42, 4, v1
	v_mul_u32_u24_e32 v42, 0x3100, v42
	v_and_b32_e32 v43, -4, v0
	v_lshl_add_u32 v42, v43, 2, v42
	ds_read_b32 v32, v42 offset:24448
	ds_read_b32 v33, v42 offset:27584
	ds_read_b32 v34, v42 offset:30720
	ds_read_b32 v35, v42 offset:33856
	ds_read_b32 v36, v42 offset:24452
	ds_read_b32 v37, v42 offset:27588
	ds_read_b32 v38, v42 offset:30724
	ds_read_b32 v39, v42 offset:33860
	ds_read_b32 v56, v42 offset:24456
	ds_read_b32 v57, v42 offset:27592
	ds_read_b32 v58, v42 offset:30728
	ds_read_b32 v59, v42 offset:33864
	ds_read_b32 v60, v42 offset:24460
	ds_read_b32 v61, v42 offset:27596
	ds_read_b32 v62, v42 offset:30732
	ds_read_b32 v63, v42 offset:33868
	s_waitcnt lgkmcnt(12)
	global_store_dwordx4 v41, v[32:35], s[68:69] nt
	s_waitcnt lgkmcnt(8)
	global_store_dwordx4 v41, v[36:39], s[68:69] offset:64 nt
	s_waitcnt lgkmcnt(4)
	global_store_dwordx4 v41, v[56:59], s[68:69] offset:128 nt
	s_waitcnt lgkmcnt(0)
	global_store_dwordx4 v41, v[60:63], s[68:69] offset:192 nt
	s_nop 1
